# baseline (speedup 1.0000x reference)
.LBB2_9:
	s_lshr_b32 s8, s14, 7
	v_and_b32_e32 v1, 15, v0
	v_bfe_u32 v98, v0, 4, 2
	s_bfe_u32 s9, s14, 0x10006
	s_and_b64 vcc, exec, s[4:5]
	s_cbranch_vccz .LBB2_13
	s_barrier
	s_cmp_lt_i32 s6, 64
	s_mov_b32 s4, 0
	s_cbranch_scc1 .LBB2_41
	v_lshrrev_b32_e32 v2, 1, v0
	v_bfe_u32 v3, v0, 1, 3
	v_bitop3_b32 v2, v98, v2, 7 bitop3:0x78
	s_mul_i32 s5, s9, 0x60
	v_lshlrev_b32_e32 v99, 4, v2
	v_bitop3_b32 v2, v98, v3, 4 bitop3:0x36
	v_or_b32_e32 v4, s5, v1
	v_lshlrev_b32_e32 v102, 4, v2
	v_mov_b32_e32 v2, 0
	s_lshl_b32 s5, s8, 13
	v_lshlrev_b32_e32 v100, 7, v1
	v_lshlrev_b32_e32 v101, 7, v4
	v_mov_b32_e32 v3, v2
	v_mov_b32_e32 v4, v2
	v_mov_b32_e32 v5, v2
	v_mov_b32_e32 v6, v2
	v_mov_b32_e32 v7, v2
	v_mov_b32_e32 v8, v2
	v_mov_b32_e32 v9, v2
	v_mov_b32_e32 v34, v2
	v_mov_b32_e32 v35, v2
	v_mov_b32_e32 v36, v2
	v_mov_b32_e32 v37, v2
	v_mov_b32_e32 v38, v2
	v_mov_b32_e32 v39, v2
	v_mov_b32_e32 v40, v2
	v_mov_b32_e32 v41, v2
	v_mov_b32_e32 v66, v2
	v_mov_b32_e32 v67, v2
	v_mov_b32_e32 v68, v2
	v_mov_b32_e32 v69, v2
	v_mov_b32_e32 v70, v2
	v_mov_b32_e32 v71, v2
	v_mov_b32_e32 v72, v2
	v_mov_b32_e32 v73, v2
	v_mov_b32_e32 v10, v2
	v_mov_b32_e32 v11, v2
	v_mov_b32_e32 v12, v2
	v_mov_b32_e32 v13, v2
	v_mov_b32_e32 v14, v2
	v_mov_b32_e32 v15, v2
	v_mov_b32_e32 v16, v2
	v_mov_b32_e32 v17, v2
	v_mov_b32_e32 v42, v2
	v_mov_b32_e32 v43, v2
	v_mov_b32_e32 v44, v2
	v_mov_b32_e32 v45, v2
	v_mov_b32_e32 v46, v2
	v_mov_b32_e32 v47, v2
	v_mov_b32_e32 v48, v2
	v_mov_b32_e32 v49, v2
	v_mov_b32_e32 v74, v2
	v_mov_b32_e32 v75, v2
	v_mov_b32_e32 v76, v2
	v_mov_b32_e32 v77, v2
	v_mov_b32_e32 v78, v2
	v_mov_b32_e32 v79, v2
	v_mov_b32_e32 v80, v2
	v_mov_b32_e32 v81, v2
	v_mov_b32_e32 v18, v2
	v_mov_b32_e32 v19, v2
	v_mov_b32_e32 v20, v2
	v_mov_b32_e32 v21, v2
	v_mov_b32_e32 v22, v2
	v_mov_b32_e32 v23, v2
	v_mov_b32_e32 v24, v2
	v_mov_b32_e32 v25, v2
	v_mov_b32_e32 v50, v2
	v_mov_b32_e32 v51, v2
	v_mov_b32_e32 v52, v2
	v_mov_b32_e32 v53, v2
	v_mov_b32_e32 v54, v2
	v_mov_b32_e32 v55, v2
	v_mov_b32_e32 v56, v2
	v_mov_b32_e32 v57, v2
	v_mov_b32_e32 v82, v2
	v_mov_b32_e32 v83, v2
	v_mov_b32_e32 v84, v2
	v_mov_b32_e32 v85, v2
	v_mov_b32_e32 v86, v2
	v_mov_b32_e32 v87, v2
	v_mov_b32_e32 v88, v2
	v_mov_b32_e32 v89, v2
	v_mov_b32_e32 v26, v2
	v_mov_b32_e32 v27, v2
	v_mov_b32_e32 v28, v2
	v_mov_b32_e32 v29, v2
	v_mov_b32_e32 v30, v2
	v_mov_b32_e32 v31, v2
	v_mov_b32_e32 v32, v2
	v_mov_b32_e32 v33, v2
	v_mov_b32_e32 v58, v2
	v_mov_b32_e32 v59, v2
	v_mov_b32_e32 v60, v2
	v_mov_b32_e32 v61, v2
	v_mov_b32_e32 v62, v2
	v_mov_b32_e32 v63, v2
	v_mov_b32_e32 v64, v2
	v_mov_b32_e32 v65, v2
	v_mov_b32_e32 v90, v2
	v_mov_b32_e32 v91, v2
	v_mov_b32_e32 v92, v2
	v_mov_b32_e32 v93, v2
	v_mov_b32_e32 v94, v2
	v_mov_b32_e32 v95, v2
	v_mov_b32_e32 v96, v2
	v_mov_b32_e32 v97, v2
	.p2align	6
